# P0 |W_in| column-max pass: 48-deep rotating load window with scalar row base (was ~5 loads in flight)
# baseline (speedup 1.0000x reference)
; __device__ __forceinline__ void p0_prologue(Frame& F) {
;     ...
;     { const float* W = F.in[I_WIN]; unsigned* colmax = F.ctl + CW_COLMAX;
;       for (int task = gw; task < 168 * 16; task += NGW) { const int cb = task % 168, kc = task / 168, n = cb * 64 + F.lane; float m = 0.f;
;           if (n < NIN) { const float* wp = W + (size_t)(kc * 128) * NIN + n;
; #pragma unroll 1
;               for (int k0 = 0; k0 < 128; k0 += 32) { float v[32];
; #pragma unroll
;                   for (int i = 0; i < 32; ++i) v[i] = wp[(size_t)(k0 + i) * NIN];
; #pragma unroll
;                   for (int i = 0; i < 32; ++i) m = fmaxf(m, fabsf(v[i])); }
;               atomicMax(colmax + n, __float_as_uint(m)); } } }
.LBB0_15:
	v_lshlrev_b32_e32 v88, 2, v2
	s_mov_b64 s[98:99], s[14:15]
	global_load_dword v40, v88, s[98:99]
	s_add_u32 s98, s98, 0xa720
	s_addc_u32 s99, s99, 0
	global_load_dword v41, v88, s[98:99]
	s_add_u32 s98, s98, 0xa720
	s_addc_u32 s99, s99, 0
	global_load_dword v42, v88, s[98:99]
	s_add_u32 s98, s98, 0xa720
	s_addc_u32 s99, s99, 0
	global_load_dword v43, v88, s[98:99]
	s_add_u32 s98, s98, 0xa720
	s_addc_u32 s99, s99, 0
	global_load_dword v44, v88, s[98:99]
	s_add_u32 s98, s98, 0xa720
	s_addc_u32 s99, s99, 0
	global_load_dword v45, v88, s[98:99]
	s_add_u32 s98, s98, 0xa720
	s_addc_u32 s99, s99, 0
	global_load_dword v46, v88, s[98:99]
	s_add_u32 s98, s98, 0xa720
	s_addc_u32 s99, s99, 0
	global_load_dword v47, v88, s[98:99]
	s_add_u32 s98, s98, 0xa720
	s_addc_u32 s99, s99, 0
	global_load_dword v48, v88, s[98:99]
	s_add_u32 s98, s98, 0xa720
	s_addc_u32 s99, s99, 0
	global_load_dword v49, v88, s[98:99]
	s_add_u32 s98, s98, 0xa720
	s_addc_u32 s99, s99, 0
	global_load_dword v50, v88, s[98:99]
	s_add_u32 s98, s98, 0xa720
	s_addc_u32 s99, s99, 0
	global_load_dword v51, v88, s[98:99]
	s_add_u32 s98, s98, 0xa720
	s_addc_u32 s99, s99, 0
	global_load_dword v52, v88, s[98:99]
	s_add_u32 s98, s98, 0xa720
	s_addc_u32 s99, s99, 0
	global_load_dword v53, v88, s[98:99]
	s_add_u32 s98, s98, 0xa720
	s_addc_u32 s99, s99, 0
	global_load_dword v54, v88, s[98:99]
	s_add_u32 s98, s98, 0xa720
	s_addc_u32 s99, s99, 0
	global_load_dword v55, v88, s[98:99]
	s_add_u32 s98, s98, 0xa720
	s_addc_u32 s99, s99, 0
	global_load_dword v56, v88, s[98:99]
	s_add_u32 s98, s98, 0xa720
	s_addc_u32 s99, s99, 0
	global_load_dword v57, v88, s[98:99]
	s_add_u32 s98, s98, 0xa720
	s_addc_u32 s99, s99, 0
	global_load_dword v58, v88, s[98:99]
	s_add_u32 s98, s98, 0xa720
	s_addc_u32 s99, s99, 0
	global_load_dword v59, v88, s[98:99]
	s_add_u32 s98, s98, 0xa720
	s_addc_u32 s99, s99, 0
	global_load_dword v60, v88, s[98:99]
	s_add_u32 s98, s98, 0xa720
	s_addc_u32 s99, s99, 0
	global_load_dword v61, v88, s[98:99]
	s_add_u32 s98, s98, 0xa720
	s_addc_u32 s99, s99, 0
	global_load_dword v62, v88, s[98:99]
	s_add_u32 s98, s98, 0xa720
	s_addc_u32 s99, s99, 0
	global_load_dword v63, v88, s[98:99]
	s_add_u32 s98, s98, 0xa720
	s_addc_u32 s99, s99, 0
	global_load_dword v64, v88, s[98:99]
	s_add_u32 s98, s98, 0xa720
	s_addc_u32 s99, s99, 0
	global_load_dword v65, v88, s[98:99]
	s_add_u32 s98, s98, 0xa720
	s_addc_u32 s99, s99, 0
	global_load_dword v66, v88, s[98:99]
	s_add_u32 s98, s98, 0xa720
	s_addc_u32 s99, s99, 0
	global_load_dword v67, v88, s[98:99]
	s_add_u32 s98, s98, 0xa720
	s_addc_u32 s99, s99, 0
	global_load_dword v68, v88, s[98:99]
	s_add_u32 s98, s98, 0xa720
	s_addc_u32 s99, s99, 0
	global_load_dword v69, v88, s[98:99]
	s_add_u32 s98, s98, 0xa720
	s_addc_u32 s99, s99, 0
	global_load_dword v70, v88, s[98:99]
	s_add_u32 s98, s98, 0xa720
	s_addc_u32 s99, s99, 0
	global_load_dword v71, v88, s[98:99]
	s_add_u32 s98, s98, 0xa720
	s_addc_u32 s99, s99, 0
	global_load_dword v72, v88, s[98:99]
	s_add_u32 s98, s98, 0xa720
	s_addc_u32 s99, s99, 0
	global_load_dword v73, v88, s[98:99]
	s_add_u32 s98, s98, 0xa720
	s_addc_u32 s99, s99, 0
	global_load_dword v74, v88, s[98:99]
	s_add_u32 s98, s98, 0xa720
	s_addc_u32 s99, s99, 0
	global_load_dword v75, v88, s[98:99]
	s_add_u32 s98, s98, 0xa720
	s_addc_u32 s99, s99, 0
	global_load_dword v76, v88, s[98:99]
	s_add_u32 s98, s98, 0xa720
	s_addc_u32 s99, s99, 0
	global_load_dword v77, v88, s[98:99]
	s_add_u32 s98, s98, 0xa720
	s_addc_u32 s99, s99, 0
	global_load_dword v78, v88, s[98:99]
	s_add_u32 s98, s98, 0xa720
	s_addc_u32 s99, s99, 0
	global_load_dword v79, v88, s[98:99]
	s_add_u32 s98, s98, 0xa720
	s_addc_u32 s99, s99, 0
	global_load_dword v80, v88, s[98:99]
	s_add_u32 s98, s98, 0xa720
	s_addc_u32 s99, s99, 0
	global_load_dword v81, v88, s[98:99]
	s_add_u32 s98, s98, 0xa720
	s_addc_u32 s99, s99, 0
	global_load_dword v82, v88, s[98:99]
	s_add_u32 s98, s98, 0xa720
	s_addc_u32 s99, s99, 0
	global_load_dword v83, v88, s[98:99]
	s_add_u32 s98, s98, 0xa720
	s_addc_u32 s99, s99, 0
	global_load_dword v84, v88, s[98:99]
	s_add_u32 s98, s98, 0xa720
	s_addc_u32 s99, s99, 0
	global_load_dword v85, v88, s[98:99]
	s_add_u32 s98, s98, 0xa720
	s_addc_u32 s99, s99, 0
	global_load_dword v86, v88, s[98:99]
	s_add_u32 s98, s98, 0xa720
	s_addc_u32 s99, s99, 0
	global_load_dword v87, v88, s[98:99]
	s_waitcnt vmcnt(46)
	v_max3_f32 v1, v1, |v40|, |v41|
	s_add_u32 s98, s98, 0xa720
	s_addc_u32 s99, s99, 0
	global_load_dword v40, v88, s[98:99]
	s_add_u32 s98, s98, 0xa720
	s_addc_u32 s99, s99, 0
	global_load_dword v41, v88, s[98:99]
	s_waitcnt vmcnt(46)
	v_max3_f32 v1, v1, |v42|, |v43|
	s_add_u32 s98, s98, 0xa720
	s_addc_u32 s99, s99, 0
	global_load_dword v42, v88, s[98:99]
	s_add_u32 s98, s98, 0xa720
	s_addc_u32 s99, s99, 0
	global_load_dword v43, v88, s[98:99]
	s_waitcnt vmcnt(46)
	v_max3_f32 v1, v1, |v44|, |v45|
	s_add_u32 s98, s98, 0xa720
	s_addc_u32 s99, s99, 0
	global_load_dword v44, v88, s[98:99]
	s_add_u32 s98, s98, 0xa720
	s_addc_u32 s99, s99, 0
	global_load_dword v45, v88, s[98:99]
	s_waitcnt vmcnt(46)
	v_max3_f32 v1, v1, |v46|, |v47|
	s_add_u32 s98, s98, 0xa720
	s_addc_u32 s99, s99, 0
	global_load_dword v46, v88, s[98:99]
	s_add_u32 s98, s98, 0xa720
	s_addc_u32 s99, s99, 0
	global_load_dword v47, v88, s[98:99]
	s_waitcnt vmcnt(46)
	v_max3_f32 v1, v1, |v48|, |v49|
	s_add_u32 s98, s98, 0xa720
	s_addc_u32 s99, s99, 0
	global_load_dword v48, v88, s[98:99]
	s_add_u32 s98, s98, 0xa720
	s_addc_u32 s99, s99, 0
	global_load_dword v49, v88, s[98:99]
	s_waitcnt vmcnt(46)
; __device__ __forceinline__ void p0_prologue(Frame& F) {
;     ...
;     { const float* W = F.in[I_WIN]; unsigned* colmax = F.ctl + CW_COLMAX;
;       for (int task = gw; task < 168 * 16; task += NGW) { const int cb = task % 168, kc = task / 168, n = cb * 64 + F.lane; float m = 0.f;
;           if (n < NIN) { const float* wp = W + (size_t)(kc * 128) * NIN + n;
; #pragma unroll 1
;               for (int k0 = 0; k0 < 128; k0 += 32) { float v[32];
; #pragma unroll
;                   for (int i = 0; i < 32; ++i) v[i] = wp[(size_t)(k0 + i) * NIN];
; #pragma unroll
;                   for (int i = 0; i < 32; ++i) m = fmaxf(m, fabsf(v[i])); }
;               atomicMax(colmax + n, __float_as_uint(m)); } } }
	v_max3_f32 v1, v1, |v50|, |v51|
	s_add_u32 s98, s98, 0xa720
	s_addc_u32 s99, s99, 0
	global_load_dword v50, v88, s[98:99]
	s_add_u32 s98, s98, 0xa720
	s_addc_u32 s99, s99, 0
	global_load_dword v51, v88, s[98:99]
	s_waitcnt vmcnt(46)
	v_max3_f32 v1, v1, |v52|, |v53|
	s_add_u32 s98, s98, 0xa720
	s_addc_u32 s99, s99, 0
	global_load_dword v52, v88, s[98:99]
	s_add_u32 s98, s98, 0xa720
	s_addc_u32 s99, s99, 0
	global_load_dword v53, v88, s[98:99]
	s_waitcnt vmcnt(46)
	v_max3_f32 v1, v1, |v54|, |v55|
	s_add_u32 s98, s98, 0xa720
	s_addc_u32 s99, s99, 0
	global_load_dword v54, v88, s[98:99]
	s_add_u32 s98, s98, 0xa720
	s_addc_u32 s99, s99, 0
	global_load_dword v55, v88, s[98:99]
	s_waitcnt vmcnt(46)
	v_max3_f32 v1, v1, |v56|, |v57|
	s_add_u32 s98, s98, 0xa720
	s_addc_u32 s99, s99, 0
	global_load_dword v56, v88, s[98:99]
	s_add_u32 s98, s98, 0xa720
	s_addc_u32 s99, s99, 0
	global_load_dword v57, v88, s[98:99]
	s_waitcnt vmcnt(46)
	v_max3_f32 v1, v1, |v58|, |v59|
	s_add_u32 s98, s98, 0xa720
	s_addc_u32 s99, s99, 0
	global_load_dword v58, v88, s[98:99]
	s_add_u32 s98, s98, 0xa720
	s_addc_u32 s99, s99, 0
	global_load_dword v59, v88, s[98:99]
	s_waitcnt vmcnt(46)
	v_max3_f32 v1, v1, |v60|, |v61|
	s_add_u32 s98, s98, 0xa720
	s_addc_u32 s99, s99, 0
	global_load_dword v60, v88, s[98:99]
	s_add_u32 s98, s98, 0xa720
	s_addc_u32 s99, s99, 0
	global_load_dword v61, v88, s[98:99]
	s_waitcnt vmcnt(46)
	v_max3_f32 v1, v1, |v62|, |v63|
	s_add_u32 s98, s98, 0xa720
	s_addc_u32 s99, s99, 0
	global_load_dword v62, v88, s[98:99]
	s_add_u32 s98, s98, 0xa720
	s_addc_u32 s99, s99, 0
	global_load_dword v63, v88, s[98:99]
	s_waitcnt vmcnt(46)
	v_max3_f32 v1, v1, |v64|, |v65|
	s_add_u32 s98, s98, 0xa720
	s_addc_u32 s99, s99, 0
	global_load_dword v64, v88, s[98:99]
	s_add_u32 s98, s98, 0xa720
	s_addc_u32 s99, s99, 0
	global_load_dword v65, v88, s[98:99]
	s_waitcnt vmcnt(46)
	v_max3_f32 v1, v1, |v66|, |v67|
	s_add_u32 s98, s98, 0xa720
	s_addc_u32 s99, s99, 0
	global_load_dword v66, v88, s[98:99]
	s_add_u32 s98, s98, 0xa720
	s_addc_u32 s99, s99, 0
	global_load_dword v67, v88, s[98:99]
	s_waitcnt vmcnt(46)
	v_max3_f32 v1, v1, |v68|, |v69|
	s_add_u32 s98, s98, 0xa720
	s_addc_u32 s99, s99, 0
	global_load_dword v68, v88, s[98:99]
	s_add_u32 s98, s98, 0xa720
	s_addc_u32 s99, s99, 0
	global_load_dword v69, v88, s[98:99]
	s_waitcnt vmcnt(46)
	v_max3_f32 v1, v1, |v70|, |v71|
	s_add_u32 s98, s98, 0xa720
	s_addc_u32 s99, s99, 0
	global_load_dword v70, v88, s[98:99]
	s_add_u32 s98, s98, 0xa720
	s_addc_u32 s99, s99, 0
	global_load_dword v71, v88, s[98:99]
	s_waitcnt vmcnt(46)
	v_max3_f32 v1, v1, |v72|, |v73|
	s_add_u32 s98, s98, 0xa720
	s_addc_u32 s99, s99, 0
	global_load_dword v72, v88, s[98:99]
	s_add_u32 s98, s98, 0xa720
	s_addc_u32 s99, s99, 0
	global_load_dword v73, v88, s[98:99]
	s_waitcnt vmcnt(46)
	v_max3_f32 v1, v1, |v74|, |v75|
	s_add_u32 s98, s98, 0xa720
	s_addc_u32 s99, s99, 0
	global_load_dword v74, v88, s[98:99]
	s_add_u32 s98, s98, 0xa720
	s_addc_u32 s99, s99, 0
	global_load_dword v75, v88, s[98:99]
	s_waitcnt vmcnt(46)
	v_max3_f32 v1, v1, |v76|, |v77|
	s_add_u32 s98, s98, 0xa720
	s_addc_u32 s99, s99, 0
	global_load_dword v76, v88, s[98:99]
	s_add_u32 s98, s98, 0xa720
	s_addc_u32 s99, s99, 0
	global_load_dword v77, v88, s[98:99]
	s_waitcnt vmcnt(46)
	v_max3_f32 v1, v1, |v78|, |v79|
	s_add_u32 s98, s98, 0xa720
	s_addc_u32 s99, s99, 0
	global_load_dword v78, v88, s[98:99]
	s_add_u32 s98, s98, 0xa720
	s_addc_u32 s99, s99, 0
	global_load_dword v79, v88, s[98:99]
	s_waitcnt vmcnt(46)
	v_max3_f32 v1, v1, |v80|, |v81|
	s_add_u32 s98, s98, 0xa720
	s_addc_u32 s99, s99, 0
	global_load_dword v80, v88, s[98:99]
	s_add_u32 s98, s98, 0xa720
	s_addc_u32 s99, s99, 0
	global_load_dword v81, v88, s[98:99]
	s_waitcnt vmcnt(46)
	v_max3_f32 v1, v1, |v82|, |v83|
	s_add_u32 s98, s98, 0xa720
	s_addc_u32 s99, s99, 0
	global_load_dword v82, v88, s[98:99]
	s_add_u32 s98, s98, 0xa720
	s_addc_u32 s99, s99, 0
	global_load_dword v83, v88, s[98:99]
	s_waitcnt vmcnt(46)
	v_max3_f32 v1, v1, |v84|, |v85|
	s_add_u32 s98, s98, 0xa720
	s_addc_u32 s99, s99, 0
	global_load_dword v84, v88, s[98:99]
	s_add_u32 s98, s98, 0xa720
	s_addc_u32 s99, s99, 0
	global_load_dword v85, v88, s[98:99]
	s_waitcnt vmcnt(46)
	v_max3_f32 v1, v1, |v86|, |v87|
	s_add_u32 s98, s98, 0xa720
	s_addc_u32 s99, s99, 0
	global_load_dword v86, v88, s[98:99]
	s_add_u32 s98, s98, 0xa720
	s_addc_u32 s99, s99, 0
	global_load_dword v87, v88, s[98:99]
	s_waitcnt vmcnt(46)
	v_max3_f32 v1, v1, |v40|, |v41|
	s_add_u32 s98, s98, 0xa720
	s_addc_u32 s99, s99, 0
	global_load_dword v40, v88, s[98:99]
	s_add_u32 s98, s98, 0xa720
	s_addc_u32 s99, s99, 0
	global_load_dword v41, v88, s[98:99]
	s_waitcnt vmcnt(46)
; __device__ __forceinline__ void p0_prologue(Frame& F) {
;     ...
;     { const float* W = F.in[I_WIN]; unsigned* colmax = F.ctl + CW_COLMAX;
;       for (int task = gw; task < 168 * 16; task += NGW) { const int cb = task % 168, kc = task / 168, n = cb * 64 + F.lane; float m = 0.f;
;           if (n < NIN) { const float* wp = W + (size_t)(kc * 128) * NIN + n;
; #pragma unroll 1
;               for (int k0 = 0; k0 < 128; k0 += 32) { float v[32];
; #pragma unroll
;                   for (int i = 0; i < 32; ++i) v[i] = wp[(size_t)(k0 + i) * NIN];
; #pragma unroll
;                   for (int i = 0; i < 32; ++i) m = fmaxf(m, fabsf(v[i])); }
;               atomicMax(colmax + n, __float_as_uint(m)); } } }
	v_max3_f32 v1, v1, |v42|, |v43|
	s_add_u32 s98, s98, 0xa720
	s_addc_u32 s99, s99, 0
	global_load_dword v42, v88, s[98:99]
	s_add_u32 s98, s98, 0xa720
	s_addc_u32 s99, s99, 0
	global_load_dword v43, v88, s[98:99]
	s_waitcnt vmcnt(46)
	v_max3_f32 v1, v1, |v44|, |v45|
	s_add_u32 s98, s98, 0xa720
	s_addc_u32 s99, s99, 0
	global_load_dword v44, v88, s[98:99]
	s_add_u32 s98, s98, 0xa720
	s_addc_u32 s99, s99, 0
	global_load_dword v45, v88, s[98:99]
	s_waitcnt vmcnt(46)
	v_max3_f32 v1, v1, |v46|, |v47|
	s_add_u32 s98, s98, 0xa720
	s_addc_u32 s99, s99, 0
	global_load_dword v46, v88, s[98:99]
	s_add_u32 s98, s98, 0xa720
	s_addc_u32 s99, s99, 0
	global_load_dword v47, v88, s[98:99]
	s_waitcnt vmcnt(46)
	v_max3_f32 v1, v1, |v48|, |v49|
	s_add_u32 s98, s98, 0xa720
	s_addc_u32 s99, s99, 0
	global_load_dword v48, v88, s[98:99]
	s_add_u32 s98, s98, 0xa720
	s_addc_u32 s99, s99, 0
	global_load_dword v49, v88, s[98:99]
	s_waitcnt vmcnt(46)
	v_max3_f32 v1, v1, |v50|, |v51|
	s_add_u32 s98, s98, 0xa720
	s_addc_u32 s99, s99, 0
	global_load_dword v50, v88, s[98:99]
	s_add_u32 s98, s98, 0xa720
	s_addc_u32 s99, s99, 0
	global_load_dword v51, v88, s[98:99]
	s_waitcnt vmcnt(46)
	v_max3_f32 v1, v1, |v52|, |v53|
	s_add_u32 s98, s98, 0xa720
	s_addc_u32 s99, s99, 0
	global_load_dword v52, v88, s[98:99]
	s_add_u32 s98, s98, 0xa720
	s_addc_u32 s99, s99, 0
	global_load_dword v53, v88, s[98:99]
	s_waitcnt vmcnt(46)
	v_max3_f32 v1, v1, |v54|, |v55|
	s_add_u32 s98, s98, 0xa720
	s_addc_u32 s99, s99, 0
	global_load_dword v54, v88, s[98:99]
	s_add_u32 s98, s98, 0xa720
	s_addc_u32 s99, s99, 0
	global_load_dword v55, v88, s[98:99]
	s_waitcnt vmcnt(46)
	v_max3_f32 v1, v1, |v56|, |v57|
	s_add_u32 s98, s98, 0xa720
	s_addc_u32 s99, s99, 0
	global_load_dword v56, v88, s[98:99]
	s_add_u32 s98, s98, 0xa720
	s_addc_u32 s99, s99, 0
	global_load_dword v57, v88, s[98:99]
	s_waitcnt vmcnt(46)
	v_max3_f32 v1, v1, |v58|, |v59|
	s_add_u32 s98, s98, 0xa720
	s_addc_u32 s99, s99, 0
	global_load_dword v58, v88, s[98:99]
	s_add_u32 s98, s98, 0xa720
	s_addc_u32 s99, s99, 0
	global_load_dword v59, v88, s[98:99]
	s_waitcnt vmcnt(46)
	v_max3_f32 v1, v1, |v60|, |v61|
	s_add_u32 s98, s98, 0xa720
	s_addc_u32 s99, s99, 0
	global_load_dword v60, v88, s[98:99]
	s_add_u32 s98, s98, 0xa720
	s_addc_u32 s99, s99, 0
	global_load_dword v61, v88, s[98:99]
	s_waitcnt vmcnt(46)
	v_max3_f32 v1, v1, |v62|, |v63|
	s_add_u32 s98, s98, 0xa720
	s_addc_u32 s99, s99, 0
	global_load_dword v62, v88, s[98:99]
	s_add_u32 s98, s98, 0xa720
	s_addc_u32 s99, s99, 0
	global_load_dword v63, v88, s[98:99]
	s_waitcnt vmcnt(46)
	v_max3_f32 v1, v1, |v64|, |v65|
	s_add_u32 s98, s98, 0xa720
	s_addc_u32 s99, s99, 0
	global_load_dword v64, v88, s[98:99]
	s_add_u32 s98, s98, 0xa720
	s_addc_u32 s99, s99, 0
	global_load_dword v65, v88, s[98:99]
	s_waitcnt vmcnt(46)
	v_max3_f32 v1, v1, |v66|, |v67|
	s_add_u32 s98, s98, 0xa720
	s_addc_u32 s99, s99, 0
	global_load_dword v66, v88, s[98:99]
	s_add_u32 s98, s98, 0xa720
	s_addc_u32 s99, s99, 0
	global_load_dword v67, v88, s[98:99]
	s_waitcnt vmcnt(46)
	v_max3_f32 v1, v1, |v68|, |v69|
	s_add_u32 s98, s98, 0xa720
	s_addc_u32 s99, s99, 0
	global_load_dword v68, v88, s[98:99]
	s_add_u32 s98, s98, 0xa720
	s_addc_u32 s99, s99, 0
	global_load_dword v69, v88, s[98:99]
	s_waitcnt vmcnt(46)
	v_max3_f32 v1, v1, |v70|, |v71|
	s_add_u32 s98, s98, 0xa720
	s_addc_u32 s99, s99, 0
	global_load_dword v70, v88, s[98:99]
	s_add_u32 s98, s98, 0xa720
	s_addc_u32 s99, s99, 0
	global_load_dword v71, v88, s[98:99]
	s_waitcnt vmcnt(46)
	v_max3_f32 v1, v1, |v72|, |v73|
	s_waitcnt vmcnt(44)
	v_max3_f32 v1, v1, |v74|, |v75|
	s_waitcnt vmcnt(42)
	v_max3_f32 v1, v1, |v76|, |v77|
	s_waitcnt vmcnt(40)
	v_max3_f32 v1, v1, |v78|, |v79|
	s_waitcnt vmcnt(38)
	v_max3_f32 v1, v1, |v80|, |v81|
	s_waitcnt vmcnt(36)
	v_max3_f32 v1, v1, |v82|, |v83|
	s_waitcnt vmcnt(34)
	v_max3_f32 v1, v1, |v84|, |v85|
	s_waitcnt vmcnt(32)
	v_max3_f32 v1, v1, |v86|, |v87|
	s_waitcnt vmcnt(30)
	v_max3_f32 v1, v1, |v40|, |v41|
	s_waitcnt vmcnt(28)
	v_max3_f32 v1, v1, |v42|, |v43|
	s_waitcnt vmcnt(26)
	v_max3_f32 v1, v1, |v44|, |v45|
	s_waitcnt vmcnt(24)
	v_max3_f32 v1, v1, |v46|, |v47|
	s_waitcnt vmcnt(22)
	v_max3_f32 v1, v1, |v48|, |v49|
	s_waitcnt vmcnt(20)
	v_max3_f32 v1, v1, |v50|, |v51|
	s_waitcnt vmcnt(18)
	v_max3_f32 v1, v1, |v52|, |v53|
	s_waitcnt vmcnt(16)
	v_max3_f32 v1, v1, |v54|, |v55|
	s_waitcnt vmcnt(14)
	v_max3_f32 v1, v1, |v56|, |v57|
	s_waitcnt vmcnt(12)
	v_max3_f32 v1, v1, |v58|, |v59|
	s_waitcnt vmcnt(10)
	v_max3_f32 v1, v1, |v60|, |v61|
	s_waitcnt vmcnt(8)
	v_max3_f32 v1, v1, |v62|, |v63|
	s_waitcnt vmcnt(6)
	v_max3_f32 v1, v1, |v64|, |v65|
	s_waitcnt vmcnt(4)
	v_max3_f32 v1, v1, |v66|, |v67|
	s_waitcnt vmcnt(2)
	v_max3_f32 v1, v1, |v68|, |v69|
	s_waitcnt vmcnt(0)
	v_max3_f32 v1, v1, |v70|, |v71|
	v_lshl_add_u64 v[2:3], v[2:3], 2, s[12:13]
	global_atomic_umax v[2:3], v1, off
	s_branch .LBB0_12
